# K-loop control arithmetic moved ahead of the iteration's last barrier (P1/P3/P5/P6) on top of the mid-epilogue align barrier; m1
# baseline (speedup 1.0000x reference)
.LBB0_240:
	ds_read_b128 v[118:121], v210
	ds_read_b128 v[122:125], v210 offset:1024
	ds_read_b128 v[130:133], v210 offset:2048
	ds_read_b128 v[134:137], v210 offset:3072
	ds_read_b128 v[146:149], v211
	ds_read_b128 v[150:153], v211 offset:1024
	ds_read_b128 v[154:157], v211 offset:2048
	ds_read_b128 v[158:161], v211 offset:3072
	s_add_i32 s8, s0, s34
	s_sub_i32 s8, s8, s20
	s_add_i32 s5, s4, s34
	s_add_i32 s18, s8, 0x7ff80
	s_cmp_eq_u32 s3, 28
	s_cselect_b64 s[8:9], -1, 0
	s_and_b64 s[14:15], s[8:9], exec
	s_cselect_b32 s14, 0, s34
	s_mov_b32 m0, s89
	ds_read_b128 v[162:165], v212
	ds_read_b128 v[166:169], v212 offset:1024
	ds_read_b128 v[170:173], v212 offset:2048
	ds_read_b128 v[174:177], v212 offset:3072
	ds_read_b128 v[178:181], v212 offset:4096
	ds_read_b128 v[182:185], v212 offset:5120
	ds_read_b128 v[186:189], v212 offset:6144
	ds_read_b128 v[190:193], v212 offset:7168
	buffer_load_dwordx4 v195, s[20:23], s18 offen lds
	s_mov_b32 m0, s90
	s_nop 0
	buffer_load_dwordx4 v205, s[20:23], s18 offen lds
	s_waitcnt vmcnt(8)
	s_waitcnt lgkmcnt(0)
	s_barrier
	v_mfma_f32_16x16x32_bf16 v[142:145], v[118:121], v[162:165], v[142:145]
	v_mfma_f32_16x16x32_bf16 v[138:141], v[130:133], v[162:165], v[138:141]
	v_mfma_f32_16x16x32_bf16 v[110:113], v[118:121], v[170:173], v[110:113]
	v_mfma_f32_16x16x32_bf16 v[106:109], v[130:133], v[170:173], v[106:109]
	v_mfma_f32_16x16x32_bf16 v[94:97], v[118:121], v[178:181], v[94:97]
	v_mfma_f32_16x16x32_bf16 v[90:93], v[130:133], v[178:181], v[90:93]
	v_mfma_f32_16x16x32_bf16 v[78:81], v[118:121], v[186:189], v[78:81]
	v_mfma_f32_16x16x32_bf16 v[74:77], v[130:133], v[186:189], v[74:77]
	v_mfma_f32_16x16x32_bf16 v[126:129], v[146:149], v[162:165], v[126:129]
	v_mfma_f32_16x16x32_bf16 v[114:117], v[154:157], v[162:165], v[114:117]
	v_mfma_f32_16x16x32_bf16 v[102:105], v[146:149], v[170:173], v[102:105]
	v_mfma_f32_16x16x32_bf16 v[98:101], v[154:157], v[170:173], v[98:101]
	v_mfma_f32_16x16x32_bf16 v[86:89], v[146:149], v[178:181], v[86:89]
	v_mfma_f32_16x16x32_bf16 v[82:85], v[154:157], v[178:181], v[82:85]
	v_mfma_f32_16x16x32_bf16 v[70:73], v[146:149], v[186:189], v[70:73]
	v_mfma_f32_16x16x32_bf16 v[66:69], v[154:157], v[186:189], v[66:69]
	v_mfma_f32_16x16x32_bf16 v[142:145], v[122:125], v[166:169], v[142:145]
	v_mfma_f32_16x16x32_bf16 v[138:141], v[134:137], v[166:169], v[138:141]
	v_mfma_f32_16x16x32_bf16 v[110:113], v[122:125], v[174:177], v[110:113]
	v_mfma_f32_16x16x32_bf16 v[106:109], v[134:137], v[174:177], v[106:109]
	v_mfma_f32_16x16x32_bf16 v[94:97], v[122:125], v[182:185], v[94:97]
	v_mfma_f32_16x16x32_bf16 v[90:93], v[134:137], v[182:185], v[90:93]
	v_mfma_f32_16x16x32_bf16 v[78:81], v[122:125], v[190:193], v[78:81]
	v_mfma_f32_16x16x32_bf16 v[74:77], v[134:137], v[190:193], v[74:77]
	v_mfma_f32_16x16x32_bf16 v[126:129], v[150:153], v[166:169], v[126:129]
	v_mfma_f32_16x16x32_bf16 v[114:117], v[158:161], v[166:169], v[114:117]
	v_mfma_f32_16x16x32_bf16 v[102:105], v[150:153], v[174:177], v[102:105]
	v_mfma_f32_16x16x32_bf16 v[98:101], v[158:161], v[174:177], v[98:101]
	v_mfma_f32_16x16x32_bf16 v[86:89], v[150:153], v[182:185], v[86:89]
	v_mfma_f32_16x16x32_bf16 v[82:85], v[158:161], v[182:185], v[82:85]
	v_mfma_f32_16x16x32_bf16 v[70:73], v[150:153], v[190:193], v[70:73]
	v_mfma_f32_16x16x32_bf16 v[66:69], v[158:161], v[190:193], v[66:69]
	s_barrier
	s_cselect_b32 s5, s1, s5
	s_sub_i32 s5, s5, s16
	s_mov_b32 m0, s52
	s_mov_b32 s18, s22
	s_mov_b32 s19, s23
	s_add_i32 s15, s5, 0x80000
	s_and_b64 s[8:9], s[86:87], s[8:9]
	ds_read_b128 v[162:165], v212 offset:16384
	ds_read_b128 v[166:169], v212 offset:17408
	ds_read_b128 v[170:173], v212 offset:18432
	ds_read_b128 v[174:177], v212 offset:19456
	ds_read_b128 v[178:181], v212 offset:20480
	ds_read_b128 v[182:185], v212 offset:21504
	ds_read_b128 v[186:189], v212 offset:22528
	ds_read_b128 v[190:193], v212 offset:23552
	buffer_load_dwordx4 v204, s[16:19], s5 offen lds
	s_mov_b32 m0, s53
	s_and_b64 s[8:9], s[8:9], exec
	buffer_load_dwordx4 v206, s[16:19], s5 offen lds
	s_mov_b32 m0, s54
	s_cselect_b32 s8, s82, s0
	buffer_load_dwordx4 v204, s[16:19], s15 offen lds
	s_mov_b32 m0, s55
	s_add_i32 s8, s8, s14
	buffer_load_dwordx4 v206, s[16:19], s15 offen lds
	s_sub_i32 s8, s8, s20
	s_mov_b32 m0, s33
	s_nop 0
	buffer_load_dwordx4 v195, s[20:23], s8 offen lds
	s_mov_b32 m0, s56
	s_nop 0
	buffer_load_dwordx4 v205, s[20:23], s8 offen lds
	s_waitcnt vmcnt(8)
	s_waitcnt lgkmcnt(0)
	s_barrier
	v_mfma_f32_16x16x32_bf16 v[62:65], v[118:121], v[162:165], v[62:65]
	v_mfma_f32_16x16x32_bf16 v[58:61], v[130:133], v[162:165], v[58:61]
	v_mfma_f32_16x16x32_bf16 v[46:49], v[118:121], v[170:173], v[46:49]
	v_mfma_f32_16x16x32_bf16 v[42:45], v[130:133], v[170:173], v[42:45]
	v_mfma_f32_16x16x32_bf16 v[30:33], v[118:121], v[178:181], v[30:33]
	v_mfma_f32_16x16x32_bf16 v[26:29], v[130:133], v[178:181], v[26:29]
	v_mfma_f32_16x16x32_bf16 v[14:17], v[118:121], v[186:189], v[14:17]
	v_mfma_f32_16x16x32_bf16 v[10:13], v[130:133], v[186:189], v[10:13]
	v_mfma_f32_16x16x32_bf16 v[54:57], v[146:149], v[162:165], v[54:57]
	v_mfma_f32_16x16x32_bf16 v[50:53], v[154:157], v[162:165], v[50:53]
	v_mfma_f32_16x16x32_bf16 v[38:41], v[146:149], v[170:173], v[38:41]
	v_mfma_f32_16x16x32_bf16 v[34:37], v[154:157], v[170:173], v[34:37]
	v_mfma_f32_16x16x32_bf16 v[22:25], v[146:149], v[178:181], v[22:25]
	v_mfma_f32_16x16x32_bf16 v[18:21], v[154:157], v[178:181], v[18:21]
	v_mfma_f32_16x16x32_bf16 v[6:9], v[146:149], v[186:189], v[6:9]
	v_mfma_f32_16x16x32_bf16 v[2:5], v[154:157], v[186:189], v[2:5]
	v_mfma_f32_16x16x32_bf16 v[62:65], v[122:125], v[166:169], v[62:65]
	v_mfma_f32_16x16x32_bf16 v[58:61], v[134:137], v[166:169], v[58:61]
	v_mfma_f32_16x16x32_bf16 v[46:49], v[122:125], v[174:177], v[46:49]
	v_mfma_f32_16x16x32_bf16 v[42:45], v[134:137], v[174:177], v[42:45]
	v_mfma_f32_16x16x32_bf16 v[30:33], v[122:125], v[182:185], v[30:33]
	v_mfma_f32_16x16x32_bf16 v[26:29], v[134:137], v[182:185], v[26:29]
	v_mfma_f32_16x16x32_bf16 v[14:17], v[122:125], v[190:193], v[14:17]
	v_mfma_f32_16x16x32_bf16 v[10:13], v[134:137], v[190:193], v[10:13]
	v_mfma_f32_16x16x32_bf16 v[54:57], v[150:153], v[166:169], v[54:57]
	v_mfma_f32_16x16x32_bf16 v[50:53], v[158:161], v[166:169], v[50:53]
	v_mfma_f32_16x16x32_bf16 v[38:41], v[150:153], v[174:177], v[38:41]
	v_mfma_f32_16x16x32_bf16 v[34:37], v[158:161], v[174:177], v[34:37]
	v_mfma_f32_16x16x32_bf16 v[22:25], v[150:153], v[182:185], v[22:25]
	v_mfma_f32_16x16x32_bf16 v[18:21], v[158:161], v[182:185], v[18:21]
	v_mfma_f32_16x16x32_bf16 v[6:9], v[150:153], v[190:193], v[6:9]
	v_mfma_f32_16x16x32_bf16 v[2:5], v[158:161], v[190:193], v[2:5]
	s_barrier
	ds_read_b128 v[118:121], v213
	ds_read_b128 v[122:125], v213 offset:1024
	ds_read_b128 v[130:133], v213 offset:2048
	ds_read_b128 v[134:137], v213 offset:3072
	ds_read_b128 v[146:149], v214
	ds_read_b128 v[150:153], v214 offset:1024
	ds_read_b128 v[154:157], v214 offset:2048
	ds_read_b128 v[158:161], v214 offset:3072
	s_add_i32 s9, s8, 0x80000
	s_mov_b32 m0, s57
	ds_read_b128 v[162:165], v212 offset:32768
	ds_read_b128 v[166:169], v212 offset:33792
	ds_read_b128 v[170:173], v212 offset:34816
	ds_read_b128 v[174:177], v212 offset:35840
	ds_read_b128 v[178:181], v212 offset:36864
	ds_read_b128 v[182:185], v212 offset:37888
	ds_read_b128 v[186:189], v212 offset:38912
	ds_read_b128 v[190:193], v212 offset:39936
	buffer_load_dwordx4 v195, s[20:23], s9 offen lds
	s_mov_b32 m0, s58
	s_nop 0
	buffer_load_dwordx4 v205, s[20:23], s9 offen lds
	s_waitcnt vmcnt(8)
	s_waitcnt lgkmcnt(0)
	s_barrier
	v_mfma_f32_16x16x32_bf16 v[142:145], v[118:121], v[162:165], v[142:145]
	v_mfma_f32_16x16x32_bf16 v[138:141], v[130:133], v[162:165], v[138:141]
	v_mfma_f32_16x16x32_bf16 v[110:113], v[118:121], v[170:173], v[110:113]
	v_mfma_f32_16x16x32_bf16 v[106:109], v[130:133], v[170:173], v[106:109]
	v_mfma_f32_16x16x32_bf16 v[94:97], v[118:121], v[178:181], v[94:97]
	v_mfma_f32_16x16x32_bf16 v[90:93], v[130:133], v[178:181], v[90:93]
	v_mfma_f32_16x16x32_bf16 v[78:81], v[118:121], v[186:189], v[78:81]
	v_mfma_f32_16x16x32_bf16 v[74:77], v[130:133], v[186:189], v[74:77]
	v_mfma_f32_16x16x32_bf16 v[126:129], v[146:149], v[162:165], v[126:129]
	v_mfma_f32_16x16x32_bf16 v[114:117], v[154:157], v[162:165], v[114:117]
	v_mfma_f32_16x16x32_bf16 v[102:105], v[146:149], v[170:173], v[102:105]
	v_mfma_f32_16x16x32_bf16 v[98:101], v[154:157], v[170:173], v[98:101]
	v_mfma_f32_16x16x32_bf16 v[86:89], v[146:149], v[178:181], v[86:89]
	v_mfma_f32_16x16x32_bf16 v[82:85], v[154:157], v[178:181], v[82:85]
	v_mfma_f32_16x16x32_bf16 v[70:73], v[146:149], v[186:189], v[70:73]
	v_mfma_f32_16x16x32_bf16 v[66:69], v[154:157], v[186:189], v[66:69]
	v_mfma_f32_16x16x32_bf16 v[142:145], v[122:125], v[166:169], v[142:145]
	v_mfma_f32_16x16x32_bf16 v[138:141], v[134:137], v[166:169], v[138:141]
	v_mfma_f32_16x16x32_bf16 v[110:113], v[122:125], v[174:177], v[110:113]
	v_mfma_f32_16x16x32_bf16 v[106:109], v[134:137], v[174:177], v[106:109]
	v_mfma_f32_16x16x32_bf16 v[94:97], v[122:125], v[182:185], v[94:97]
	v_mfma_f32_16x16x32_bf16 v[90:93], v[134:137], v[182:185], v[90:93]
	v_mfma_f32_16x16x32_bf16 v[78:81], v[122:125], v[190:193], v[78:81]
	v_mfma_f32_16x16x32_bf16 v[74:77], v[134:137], v[190:193], v[74:77]
	v_mfma_f32_16x16x32_bf16 v[126:129], v[150:153], v[166:169], v[126:129]
	v_mfma_f32_16x16x32_bf16 v[114:117], v[158:161], v[166:169], v[114:117]
	v_mfma_f32_16x16x32_bf16 v[102:105], v[150:153], v[174:177], v[102:105]
	v_mfma_f32_16x16x32_bf16 v[98:101], v[158:161], v[174:177], v[98:101]
	v_mfma_f32_16x16x32_bf16 v[86:89], v[150:153], v[182:185], v[86:89]
	v_mfma_f32_16x16x32_bf16 v[82:85], v[158:161], v[182:185], v[82:85]
	v_mfma_f32_16x16x32_bf16 v[70:73], v[150:153], v[190:193], v[70:73]
	v_mfma_f32_16x16x32_bf16 v[66:69], v[158:161], v[190:193], v[66:69]
	s_barrier
	s_mov_b32 m0, s62
	s_add_i32 s9, s5, 0x80
	ds_read_b128 v[162:165], v212 offset:49152
	ds_read_b128 v[166:169], v212 offset:50176
	ds_read_b128 v[170:173], v212 offset:51200
	ds_read_b128 v[174:177], v212 offset:52224
	ds_read_b128 v[178:181], v212 offset:53248
	ds_read_b128 v[182:185], v212 offset:54272
	ds_read_b128 v[186:189], v212 offset:55296
	ds_read_b128 v[190:193], v212 offset:56320
	buffer_load_dwordx4 v204, s[16:19], s9 offen lds
	s_mov_b32 m0, s63
	s_add_i32 s5, s5, 0x80080
	buffer_load_dwordx4 v206, s[16:19], s9 offen lds
	s_mov_b32 m0, s75
	s_addk_i32 s8, 0x80
	buffer_load_dwordx4 v204, s[16:19], s5 offen lds
	s_mov_b32 m0, s88
	s_nop 0
	buffer_load_dwordx4 v206, s[16:19], s5 offen lds
	s_mov_b32 m0, s68
	s_nop 0
	buffer_load_dwordx4 v195, s[20:23], s8 offen lds
	s_mov_b32 m0, s69
	s_nop 0
	buffer_load_dwordx4 v205, s[20:23], s8 offen lds
	s_add_i32 s3, s3, 2
	s_add_u32 s34, s34, 0x100
	s_addc_u32 s35, s35, 0
	s_cmp_lt_u32 s3, 30
	s_waitcnt vmcnt(8)
	s_waitcnt lgkmcnt(0)
	s_barrier
	v_mfma_f32_16x16x32_bf16 v[62:65], v[118:121], v[162:165], v[62:65]
	v_mfma_f32_16x16x32_bf16 v[58:61], v[130:133], v[162:165], v[58:61]
	v_mfma_f32_16x16x32_bf16 v[46:49], v[118:121], v[170:173], v[46:49]
	v_mfma_f32_16x16x32_bf16 v[42:45], v[130:133], v[170:173], v[42:45]
	v_mfma_f32_16x16x32_bf16 v[30:33], v[118:121], v[178:181], v[30:33]
	v_mfma_f32_16x16x32_bf16 v[26:29], v[130:133], v[178:181], v[26:29]
	v_mfma_f32_16x16x32_bf16 v[14:17], v[118:121], v[186:189], v[14:17]
	v_mfma_f32_16x16x32_bf16 v[10:13], v[130:133], v[186:189], v[10:13]
	v_mfma_f32_16x16x32_bf16 v[54:57], v[146:149], v[162:165], v[54:57]
	v_mfma_f32_16x16x32_bf16 v[50:53], v[154:157], v[162:165], v[50:53]
	v_mfma_f32_16x16x32_bf16 v[38:41], v[146:149], v[170:173], v[38:41]
	v_mfma_f32_16x16x32_bf16 v[34:37], v[154:157], v[170:173], v[34:37]
	v_mfma_f32_16x16x32_bf16 v[22:25], v[146:149], v[178:181], v[22:25]
	v_mfma_f32_16x16x32_bf16 v[18:21], v[154:157], v[178:181], v[18:21]
	v_mfma_f32_16x16x32_bf16 v[6:9], v[146:149], v[186:189], v[6:9]
	v_mfma_f32_16x16x32_bf16 v[2:5], v[154:157], v[186:189], v[2:5]
	v_mfma_f32_16x16x32_bf16 v[62:65], v[122:125], v[166:169], v[62:65]
	v_mfma_f32_16x16x32_bf16 v[58:61], v[134:137], v[166:169], v[58:61]
	v_mfma_f32_16x16x32_bf16 v[46:49], v[122:125], v[174:177], v[46:49]
	v_mfma_f32_16x16x32_bf16 v[42:45], v[134:137], v[174:177], v[42:45]
	v_mfma_f32_16x16x32_bf16 v[30:33], v[122:125], v[182:185], v[30:33]
	v_mfma_f32_16x16x32_bf16 v[26:29], v[134:137], v[182:185], v[26:29]
	v_mfma_f32_16x16x32_bf16 v[14:17], v[122:125], v[190:193], v[14:17]
	v_mfma_f32_16x16x32_bf16 v[10:13], v[134:137], v[190:193], v[10:13]
	v_mfma_f32_16x16x32_bf16 v[54:57], v[150:153], v[166:169], v[54:57]
	v_mfma_f32_16x16x32_bf16 v[50:53], v[158:161], v[166:169], v[50:53]
	v_mfma_f32_16x16x32_bf16 v[38:41], v[150:153], v[174:177], v[38:41]
	v_mfma_f32_16x16x32_bf16 v[34:37], v[158:161], v[174:177], v[34:37]
	v_mfma_f32_16x16x32_bf16 v[22:25], v[150:153], v[182:185], v[22:25]
	v_mfma_f32_16x16x32_bf16 v[18:21], v[158:161], v[182:185], v[18:21]
	v_mfma_f32_16x16x32_bf16 v[6:9], v[150:153], v[190:193], v[6:9]
	v_mfma_f32_16x16x32_bf16 v[2:5], v[158:161], v[190:193], v[2:5]
	s_barrier
	s_cbranch_scc1 .LBB0_240
	s_andn2_b64 vcc, exec, s[70:71]
	s_cbranch_vccnz .LBB0_243
	s_barrier

.LBB0_816:
	ds_read_b128 v[132:135], v148
	ds_read_b128 v[136:139], v148 offset:1024
	ds_read_b128 v[154:157], v148 offset:2048
	ds_read_b128 v[158:161], v148 offset:3072
	ds_read_b128 v[162:165], v149
	ds_read_b128 v[166:169], v149 offset:1024
	ds_read_b128 v[170:173], v149 offset:2048
	ds_read_b128 v[174:177], v149 offset:3072
	s_add_i32 s6, s36, s44
	s_sub_i32 s6, s6, s16
	s_add_i32 s14, s38, s44
	s_add_i32 s15, s6, 0x7ff80
	s_cmp_eq_u32 s25, 28
	s_cselect_b64 s[8:9], -1, 0
	s_and_b64 s[6:7], s[8:9], exec
	s_cselect_b32 s37, 0, s44
	s_mov_b32 m0, s67
	ds_read_b128 v[178:181], v150
	ds_read_b128 v[182:185], v150 offset:1024
	ds_read_b128 v[186:189], v150 offset:2048
	ds_read_b128 v[190:193], v150 offset:3072
	ds_read_b128 v[196:199], v150 offset:4096
	ds_read_b128 v[200:203], v150 offset:5120
	ds_read_b128 v[204:207], v150 offset:6144
	ds_read_b128 v[208:211], v150 offset:7168
	buffer_load_dwordx4 v142, s[16:19], s15 offen lds
	s_mov_b32 m0, s68
	s_nop 0
	buffer_load_dwordx4 v144, s[16:19], s15 offen lds
	s_waitcnt vmcnt(8)
	s_waitcnt lgkmcnt(0)
	s_barrier
	v_mfma_f32_16x16x32_bf16 v[126:129], v[132:135], v[178:181], v[126:129]
	v_mfma_f32_16x16x32_bf16 v[122:125], v[154:157], v[178:181], v[122:125]
	v_mfma_f32_16x16x32_bf16 v[118:121], v[132:135], v[186:189], v[118:121]
	v_mfma_f32_16x16x32_bf16 v[114:117], v[154:157], v[186:189], v[114:117]
	v_mfma_f32_16x16x32_bf16 v[98:101], v[132:135], v[196:199], v[98:101]
	v_mfma_f32_16x16x32_bf16 v[90:93], v[154:157], v[196:199], v[90:93]
	v_mfma_f32_16x16x32_bf16 v[82:85], v[132:135], v[204:207], v[82:85]
	v_mfma_f32_16x16x32_bf16 v[74:77], v[154:157], v[204:207], v[74:77]
	v_mfma_f32_16x16x32_bf16 v[110:113], v[162:165], v[178:181], v[110:113]
	v_mfma_f32_16x16x32_bf16 v[106:109], v[170:173], v[178:181], v[106:109]
	v_mfma_f32_16x16x32_bf16 v[102:105], v[162:165], v[186:189], v[102:105]
	v_mfma_f32_16x16x32_bf16 v[94:97], v[170:173], v[186:189], v[94:97]
	v_mfma_f32_16x16x32_bf16 v[86:89], v[162:165], v[196:199], v[86:89]
	v_mfma_f32_16x16x32_bf16 v[78:81], v[170:173], v[196:199], v[78:81]
	v_mfma_f32_16x16x32_bf16 v[70:73], v[162:165], v[204:207], v[70:73]
	v_mfma_f32_16x16x32_bf16 v[66:69], v[170:173], v[204:207], v[66:69]
	v_mfma_f32_16x16x32_bf16 v[126:129], v[136:139], v[182:185], v[126:129]
	v_mfma_f32_16x16x32_bf16 v[122:125], v[158:161], v[182:185], v[122:125]
	v_mfma_f32_16x16x32_bf16 v[118:121], v[136:139], v[190:193], v[118:121]
	v_mfma_f32_16x16x32_bf16 v[114:117], v[158:161], v[190:193], v[114:117]
	v_mfma_f32_16x16x32_bf16 v[98:101], v[136:139], v[200:203], v[98:101]
	v_mfma_f32_16x16x32_bf16 v[90:93], v[158:161], v[200:203], v[90:93]
	v_mfma_f32_16x16x32_bf16 v[82:85], v[136:139], v[208:211], v[82:85]
	v_mfma_f32_16x16x32_bf16 v[74:77], v[158:161], v[208:211], v[74:77]
	v_mfma_f32_16x16x32_bf16 v[110:113], v[166:169], v[182:185], v[110:113]
	v_mfma_f32_16x16x32_bf16 v[106:109], v[174:177], v[182:185], v[106:109]
	v_mfma_f32_16x16x32_bf16 v[102:105], v[166:169], v[190:193], v[102:105]
	v_mfma_f32_16x16x32_bf16 v[94:97], v[174:177], v[190:193], v[94:97]
	v_mfma_f32_16x16x32_bf16 v[86:89], v[166:169], v[200:203], v[86:89]
	v_mfma_f32_16x16x32_bf16 v[78:81], v[174:177], v[200:203], v[78:81]
	v_mfma_f32_16x16x32_bf16 v[70:73], v[166:169], v[208:211], v[70:73]
	v_mfma_f32_16x16x32_bf16 v[66:69], v[174:177], v[208:211], v[66:69]
	s_barrier
	s_cselect_b32 s14, s23, s14
	s_sub_i32 s14, s14, s4
	s_mov_b32 m0, s52
	s_mov_b32 s6, s18
	s_mov_b32 s7, s19
	s_add_i32 s15, s14, 0x80000
	s_and_b64 s[8:9], s[30:31], s[8:9]
	ds_read_b128 v[178:181], v150 offset:16384
	ds_read_b128 v[182:185], v150 offset:17408
	ds_read_b128 v[186:189], v150 offset:18432
	ds_read_b128 v[190:193], v150 offset:19456
	ds_read_b128 v[196:199], v150 offset:20480
	ds_read_b128 v[200:203], v150 offset:21504
	ds_read_b128 v[204:207], v150 offset:22528
	ds_read_b128 v[208:211], v150 offset:23552
	buffer_load_dwordx4 v143, s[4:7], s14 offen lds
	s_mov_b32 m0, s53
	s_and_b64 s[8:9], s[8:9], exec
	buffer_load_dwordx4 v145, s[4:7], s14 offen lds
	s_mov_b32 m0, s54
	s_cselect_b32 s8, s26, s36
	buffer_load_dwordx4 v143, s[4:7], s15 offen lds
	s_mov_b32 m0, s55
	s_add_i32 s8, s8, s37
	buffer_load_dwordx4 v145, s[4:7], s15 offen lds
	s_sub_i32 s8, s8, s16
	s_mov_b32 m0, s35
	s_nop 0
	buffer_load_dwordx4 v142, s[16:19], s8 offen lds
	s_mov_b32 m0, s56
	s_nop 0
	buffer_load_dwordx4 v144, s[16:19], s8 offen lds
	s_waitcnt vmcnt(8)
	s_waitcnt lgkmcnt(0)
	s_barrier
	v_mfma_f32_16x16x32_bf16 v[62:65], v[132:135], v[178:181], v[62:65]
	v_mfma_f32_16x16x32_bf16 v[58:61], v[154:157], v[178:181], v[58:61]
	v_mfma_f32_16x16x32_bf16 v[54:57], v[132:135], v[186:189], v[54:57]
	v_mfma_f32_16x16x32_bf16 v[46:49], v[154:157], v[186:189], v[46:49]
	v_mfma_f32_16x16x32_bf16 v[38:41], v[132:135], v[196:199], v[38:41]
	v_mfma_f32_16x16x32_bf16 v[30:33], v[154:157], v[196:199], v[30:33]
	v_mfma_f32_16x16x32_bf16 v[22:25], v[132:135], v[204:207], v[22:25]
	v_mfma_f32_16x16x32_bf16 v[14:17], v[154:157], v[204:207], v[14:17]
	v_mfma_f32_16x16x32_bf16 v[50:53], v[162:165], v[178:181], v[50:53]
	v_mfma_f32_16x16x32_bf16 v[42:45], v[170:173], v[178:181], v[42:45]
	v_mfma_f32_16x16x32_bf16 v[34:37], v[162:165], v[186:189], v[34:37]
	v_mfma_f32_16x16x32_bf16 v[26:29], v[170:173], v[186:189], v[26:29]
	v_mfma_f32_16x16x32_bf16 v[18:21], v[162:165], v[196:199], v[18:21]
	v_mfma_f32_16x16x32_bf16 v[10:13], v[170:173], v[196:199], v[10:13]
	v_mfma_f32_16x16x32_bf16 v[6:9], v[162:165], v[204:207], v[6:9]
	v_mfma_f32_16x16x32_bf16 v[2:5], v[170:173], v[204:207], v[2:5]
	v_mfma_f32_16x16x32_bf16 v[62:65], v[136:139], v[182:185], v[62:65]
	v_mfma_f32_16x16x32_bf16 v[58:61], v[158:161], v[182:185], v[58:61]
	v_mfma_f32_16x16x32_bf16 v[54:57], v[136:139], v[190:193], v[54:57]
	v_mfma_f32_16x16x32_bf16 v[46:49], v[158:161], v[190:193], v[46:49]
	v_mfma_f32_16x16x32_bf16 v[38:41], v[136:139], v[200:203], v[38:41]
	v_mfma_f32_16x16x32_bf16 v[30:33], v[158:161], v[200:203], v[30:33]
	v_mfma_f32_16x16x32_bf16 v[22:25], v[136:139], v[208:211], v[22:25]
	v_mfma_f32_16x16x32_bf16 v[14:17], v[158:161], v[208:211], v[14:17]
	v_mfma_f32_16x16x32_bf16 v[50:53], v[166:169], v[182:185], v[50:53]
	v_mfma_f32_16x16x32_bf16 v[42:45], v[174:177], v[182:185], v[42:45]
	v_mfma_f32_16x16x32_bf16 v[34:37], v[166:169], v[190:193], v[34:37]
	v_mfma_f32_16x16x32_bf16 v[26:29], v[174:177], v[190:193], v[26:29]
	v_mfma_f32_16x16x32_bf16 v[18:21], v[166:169], v[200:203], v[18:21]
	v_mfma_f32_16x16x32_bf16 v[10:13], v[174:177], v[200:203], v[10:13]
	v_mfma_f32_16x16x32_bf16 v[6:9], v[166:169], v[208:211], v[6:9]
	v_mfma_f32_16x16x32_bf16 v[2:5], v[174:177], v[208:211], v[2:5]
	s_barrier
	ds_read_b128 v[132:135], v151
	ds_read_b128 v[136:139], v151 offset:1024
	ds_read_b128 v[154:157], v151 offset:2048
	ds_read_b128 v[158:161], v151 offset:3072
	ds_read_b128 v[162:165], v152
	ds_read_b128 v[166:169], v152 offset:1024
	ds_read_b128 v[170:173], v152 offset:2048
	ds_read_b128 v[174:177], v152 offset:3072
	s_add_i32 s9, s8, 0x80000
	s_mov_b32 m0, s57
	ds_read_b128 v[178:181], v150 offset:32768
	ds_read_b128 v[182:185], v150 offset:33792
	ds_read_b128 v[186:189], v150 offset:34816
	ds_read_b128 v[190:193], v150 offset:35840
	ds_read_b128 v[196:199], v150 offset:36864
	ds_read_b128 v[200:203], v150 offset:37888
	ds_read_b128 v[204:207], v150 offset:38912
	ds_read_b128 v[208:211], v150 offset:39936
	buffer_load_dwordx4 v142, s[16:19], s9 offen lds
	s_mov_b32 m0, s58
	s_nop 0
	buffer_load_dwordx4 v144, s[16:19], s9 offen lds
	s_waitcnt vmcnt(8)
	s_waitcnt lgkmcnt(0)
	s_barrier
	v_mfma_f32_16x16x32_bf16 v[126:129], v[132:135], v[178:181], v[126:129]
	v_mfma_f32_16x16x32_bf16 v[122:125], v[154:157], v[178:181], v[122:125]
	v_mfma_f32_16x16x32_bf16 v[118:121], v[132:135], v[186:189], v[118:121]
	v_mfma_f32_16x16x32_bf16 v[114:117], v[154:157], v[186:189], v[114:117]
	v_mfma_f32_16x16x32_bf16 v[98:101], v[132:135], v[196:199], v[98:101]
	v_mfma_f32_16x16x32_bf16 v[90:93], v[154:157], v[196:199], v[90:93]
	v_mfma_f32_16x16x32_bf16 v[82:85], v[132:135], v[204:207], v[82:85]
	v_mfma_f32_16x16x32_bf16 v[74:77], v[154:157], v[204:207], v[74:77]
	v_mfma_f32_16x16x32_bf16 v[110:113], v[162:165], v[178:181], v[110:113]
	v_mfma_f32_16x16x32_bf16 v[106:109], v[170:173], v[178:181], v[106:109]
	v_mfma_f32_16x16x32_bf16 v[102:105], v[162:165], v[186:189], v[102:105]
	v_mfma_f32_16x16x32_bf16 v[94:97], v[170:173], v[186:189], v[94:97]
	v_mfma_f32_16x16x32_bf16 v[86:89], v[162:165], v[196:199], v[86:89]
	v_mfma_f32_16x16x32_bf16 v[78:81], v[170:173], v[196:199], v[78:81]
	v_mfma_f32_16x16x32_bf16 v[70:73], v[162:165], v[204:207], v[70:73]
	v_mfma_f32_16x16x32_bf16 v[66:69], v[170:173], v[204:207], v[66:69]
	v_mfma_f32_16x16x32_bf16 v[126:129], v[136:139], v[182:185], v[126:129]
	v_mfma_f32_16x16x32_bf16 v[122:125], v[158:161], v[182:185], v[122:125]
	v_mfma_f32_16x16x32_bf16 v[118:121], v[136:139], v[190:193], v[118:121]
	v_mfma_f32_16x16x32_bf16 v[114:117], v[158:161], v[190:193], v[114:117]
	v_mfma_f32_16x16x32_bf16 v[98:101], v[136:139], v[200:203], v[98:101]
	v_mfma_f32_16x16x32_bf16 v[90:93], v[158:161], v[200:203], v[90:93]
	v_mfma_f32_16x16x32_bf16 v[82:85], v[136:139], v[208:211], v[82:85]
	v_mfma_f32_16x16x32_bf16 v[74:77], v[158:161], v[208:211], v[74:77]
	v_mfma_f32_16x16x32_bf16 v[110:113], v[166:169], v[182:185], v[110:113]
	v_mfma_f32_16x16x32_bf16 v[106:109], v[174:177], v[182:185], v[106:109]
	v_mfma_f32_16x16x32_bf16 v[102:105], v[166:169], v[190:193], v[102:105]
	v_mfma_f32_16x16x32_bf16 v[94:97], v[174:177], v[190:193], v[94:97]
	v_mfma_f32_16x16x32_bf16 v[86:89], v[166:169], v[200:203], v[86:89]
	v_mfma_f32_16x16x32_bf16 v[78:81], v[174:177], v[200:203], v[78:81]
	v_mfma_f32_16x16x32_bf16 v[70:73], v[166:169], v[208:211], v[70:73]
	v_mfma_f32_16x16x32_bf16 v[66:69], v[174:177], v[208:211], v[66:69]
	s_barrier
	s_mov_b32 m0, s61
	s_add_i32 s9, s14, 0x80
	ds_read_b128 v[178:181], v150 offset:49152
	ds_read_b128 v[182:185], v150 offset:50176
	ds_read_b128 v[186:189], v150 offset:51200
	ds_read_b128 v[190:193], v150 offset:52224
	ds_read_b128 v[196:199], v150 offset:53248
	ds_read_b128 v[200:203], v150 offset:54272
	ds_read_b128 v[204:207], v150 offset:55296
	ds_read_b128 v[208:211], v150 offset:56320
	buffer_load_dwordx4 v143, s[4:7], s9 offen lds
	s_mov_b32 m0, s62
	s_add_i32 s14, s14, 0x80080
	buffer_load_dwordx4 v145, s[4:7], s9 offen lds
	s_mov_b32 m0, s65
	s_addk_i32 s8, 0x80
	buffer_load_dwordx4 v143, s[4:7], s14 offen lds
	s_mov_b32 m0, s66
	s_nop 0
	buffer_load_dwordx4 v145, s[4:7], s14 offen lds
	s_mov_b32 m0, s63
	s_nop 0
	buffer_load_dwordx4 v142, s[16:19], s8 offen lds
	s_mov_b32 m0, s64
	s_nop 0
	buffer_load_dwordx4 v144, s[16:19], s8 offen lds
	s_add_i32 s25, s25, 2
	s_add_u32 s44, s44, 0x100
	s_addc_u32 s45, s45, 0
	s_cmp_lt_u32 s25, 30
	s_waitcnt vmcnt(8)
	s_waitcnt lgkmcnt(0)
	s_barrier
	v_mfma_f32_16x16x32_bf16 v[62:65], v[132:135], v[178:181], v[62:65]
	v_mfma_f32_16x16x32_bf16 v[58:61], v[154:157], v[178:181], v[58:61]
	v_mfma_f32_16x16x32_bf16 v[54:57], v[132:135], v[186:189], v[54:57]
	v_mfma_f32_16x16x32_bf16 v[46:49], v[154:157], v[186:189], v[46:49]
	v_mfma_f32_16x16x32_bf16 v[38:41], v[132:135], v[196:199], v[38:41]
	v_mfma_f32_16x16x32_bf16 v[30:33], v[154:157], v[196:199], v[30:33]
	v_mfma_f32_16x16x32_bf16 v[22:25], v[132:135], v[204:207], v[22:25]
	v_mfma_f32_16x16x32_bf16 v[14:17], v[154:157], v[204:207], v[14:17]
	v_mfma_f32_16x16x32_bf16 v[50:53], v[162:165], v[178:181], v[50:53]
	v_mfma_f32_16x16x32_bf16 v[42:45], v[170:173], v[178:181], v[42:45]
	v_mfma_f32_16x16x32_bf16 v[34:37], v[162:165], v[186:189], v[34:37]
	v_mfma_f32_16x16x32_bf16 v[26:29], v[170:173], v[186:189], v[26:29]
	v_mfma_f32_16x16x32_bf16 v[18:21], v[162:165], v[196:199], v[18:21]
	v_mfma_f32_16x16x32_bf16 v[10:13], v[170:173], v[196:199], v[10:13]
	v_mfma_f32_16x16x32_bf16 v[6:9], v[162:165], v[204:207], v[6:9]
	v_mfma_f32_16x16x32_bf16 v[2:5], v[170:173], v[204:207], v[2:5]
	v_mfma_f32_16x16x32_bf16 v[62:65], v[136:139], v[182:185], v[62:65]
	v_mfma_f32_16x16x32_bf16 v[58:61], v[158:161], v[182:185], v[58:61]
	v_mfma_f32_16x16x32_bf16 v[54:57], v[136:139], v[190:193], v[54:57]
	v_mfma_f32_16x16x32_bf16 v[46:49], v[158:161], v[190:193], v[46:49]
	v_mfma_f32_16x16x32_bf16 v[38:41], v[136:139], v[200:203], v[38:41]
	v_mfma_f32_16x16x32_bf16 v[30:33], v[158:161], v[200:203], v[30:33]
	v_mfma_f32_16x16x32_bf16 v[22:25], v[136:139], v[208:211], v[22:25]
	v_mfma_f32_16x16x32_bf16 v[14:17], v[158:161], v[208:211], v[14:17]
	v_mfma_f32_16x16x32_bf16 v[50:53], v[166:169], v[182:185], v[50:53]
	v_mfma_f32_16x16x32_bf16 v[42:45], v[174:177], v[182:185], v[42:45]
	v_mfma_f32_16x16x32_bf16 v[34:37], v[166:169], v[190:193], v[34:37]
	v_mfma_f32_16x16x32_bf16 v[26:29], v[174:177], v[190:193], v[26:29]
	v_mfma_f32_16x16x32_bf16 v[18:21], v[166:169], v[200:203], v[18:21]
	v_mfma_f32_16x16x32_bf16 v[10:13], v[174:177], v[200:203], v[10:13]
	v_mfma_f32_16x16x32_bf16 v[6:9], v[166:169], v[208:211], v[6:9]
	v_mfma_f32_16x16x32_bf16 v[2:5], v[174:177], v[208:211], v[2:5]
	s_barrier
	s_cbranch_scc1 .LBB0_816
	s_andn2_b64 vcc, exec, s[20:21]
	s_cbranch_vccnz .LBB0_819
	s_barrier

.LBB0_1246:
	v_add_u32_e32 v141, 0, v157
	v_add_u32_e32 v153, 0x10000, v141
	ds_read_b128 v[142:145], v153
	ds_read_b128 v[172:175], v153 offset:1024
	ds_read_b128 v[176:179], v153 offset:2048
	ds_read_b128 v[180:183], v153 offset:3072
	v_add_u32_e32 v153, 0x14000, v141
	ds_read_b128 v[184:187], v153
	ds_read_b128 v[188:191], v153 offset:1024
	ds_read_b128 v[196:199], v153 offset:2048
	ds_read_b128 v[200:203], v153 offset:3072
	s_add_u32 s38, s18, 0x100
	s_addc_u32 s39, s19, 0
	s_add_i32 s85, s29, s18
	s_and_b64 s[14:15], s[42:43], exec
	s_cselect_b32 s45, 0, s38
	s_add_i32 s14, s18, 0x80
	v_add_u32_e32 v153, 0, v156
	s_mov_b32 m0, s79
	ds_read_b128 v[204:207], v153
	ds_read_b128 v[208:211], v153 offset:1024
	ds_read_b128 v[212:215], v153 offset:2048
	ds_read_b128 v[216:219], v153 offset:3072
	ds_read_b128 v[220:223], v153 offset:4096
	ds_read_b128 v[224:227], v153 offset:5120
	ds_read_b128 v[228:231], v153 offset:6144
	ds_read_b128 v[232:235], v153 offset:7168
	buffer_load_dwordx4 v132, s[8:11], s14 offen lds
	s_mov_b32 m0, s80
	s_nop 0
	buffer_load_dwordx4 v134, s[8:11], s14 offen lds
	s_waitcnt vmcnt(8)
	s_waitcnt lgkmcnt(0)
	s_barrier
	v_mfma_f32_16x16x32_bf16 v[126:129], v[142:145], v[204:207], v[126:129]
	v_mfma_f32_16x16x32_bf16 v[122:125], v[176:179], v[204:207], v[122:125]
	v_mfma_f32_16x16x32_bf16 v[102:105], v[142:145], v[212:215], v[102:105]
	v_mfma_f32_16x16x32_bf16 v[90:93], v[176:179], v[212:215], v[90:93]
	v_mfma_f32_16x16x32_bf16 v[70:73], v[142:145], v[220:223], v[70:73]
	v_mfma_f32_16x16x32_bf16 v[58:61], v[176:179], v[220:223], v[58:61]
	v_mfma_f32_16x16x32_bf16 v[38:41], v[142:145], v[228:231], v[38:41]
	v_mfma_f32_16x16x32_bf16 v[26:29], v[176:179], v[228:231], v[26:29]
	v_mfma_f32_16x16x32_bf16 v[118:121], v[184:187], v[204:207], v[118:121]
	v_mfma_f32_16x16x32_bf16 v[110:113], v[196:199], v[204:207], v[110:113]
	v_mfma_f32_16x16x32_bf16 v[86:89], v[184:187], v[212:215], v[86:89]
	v_mfma_f32_16x16x32_bf16 v[74:77], v[196:199], v[212:215], v[74:77]
	v_mfma_f32_16x16x32_bf16 v[54:57], v[184:187], v[220:223], v[54:57]
	v_mfma_f32_16x16x32_bf16 v[42:45], v[196:199], v[220:223], v[42:45]
	v_mfma_f32_16x16x32_bf16 v[22:25], v[184:187], v[228:231], v[22:25]
	v_mfma_f32_16x16x32_bf16 v[10:13], v[196:199], v[228:231], v[10:13]
	v_mfma_f32_16x16x32_bf16 v[126:129], v[172:175], v[208:211], v[126:129]
	v_mfma_f32_16x16x32_bf16 v[122:125], v[180:183], v[208:211], v[122:125]
	v_mfma_f32_16x16x32_bf16 v[102:105], v[172:175], v[216:219], v[102:105]
	v_mfma_f32_16x16x32_bf16 v[90:93], v[180:183], v[216:219], v[90:93]
	v_mfma_f32_16x16x32_bf16 v[70:73], v[172:175], v[224:227], v[70:73]
	v_mfma_f32_16x16x32_bf16 v[58:61], v[180:183], v[224:227], v[58:61]
	v_mfma_f32_16x16x32_bf16 v[38:41], v[172:175], v[232:235], v[38:41]
	v_mfma_f32_16x16x32_bf16 v[26:29], v[180:183], v[232:235], v[26:29]
	v_mfma_f32_16x16x32_bf16 v[118:121], v[188:191], v[208:211], v[118:121]
	v_mfma_f32_16x16x32_bf16 v[110:113], v[200:203], v[208:211], v[110:113]
	v_mfma_f32_16x16x32_bf16 v[86:89], v[188:191], v[216:219], v[86:89]
	v_mfma_f32_16x16x32_bf16 v[74:77], v[200:203], v[216:219], v[74:77]
	v_mfma_f32_16x16x32_bf16 v[54:57], v[188:191], v[224:227], v[54:57]
	v_mfma_f32_16x16x32_bf16 v[42:45], v[200:203], v[224:227], v[42:45]
	v_mfma_f32_16x16x32_bf16 v[22:25], v[188:191], v[232:235], v[22:25]
	v_mfma_f32_16x16x32_bf16 v[10:13], v[200:203], v[232:235], v[10:13]
	s_barrier
	s_and_b64 s[14:15], s[42:43], exec
	s_cselect_b32 s14, s5, s85
	s_mov_b32 m0, s66
	s_mov_b32 s18, s10
	s_mov_b32 s19, s11
	s_sub_i32 s14, s14, s16
	ds_read_b128 v[204:207], v153 offset:16384
	ds_read_b128 v[208:211], v153 offset:17408
	ds_read_b128 v[212:215], v153 offset:18432
	ds_read_b128 v[216:219], v153 offset:19456
	ds_read_b128 v[220:223], v153 offset:20480
	ds_read_b128 v[224:227], v153 offset:21504
	ds_read_b128 v[228:231], v153 offset:22528
	ds_read_b128 v[232:235], v153 offset:23552
	buffer_load_dwordx4 v151, s[16:19], s14 offen lds
	s_mov_b32 m0, s67
	s_add_i32 s15, s14, 0x80000
	buffer_load_dwordx4 v158, s[16:19], s14 offen lds
	s_mov_b32 m0, s68
	s_nop 0
	buffer_load_dwordx4 v151, s[16:19], s15 offen lds
	s_mov_b32 m0, s69
	s_nop 0
	buffer_load_dwordx4 v158, s[16:19], s15 offen lds
	s_mov_b32 m0, s65
	s_nop 0
	buffer_load_dwordx4 v138, s[8:11], s45 offen lds
	s_mov_b32 m0, s70
	s_nop 0
	buffer_load_dwordx4 v137, s[8:11], s45 offen lds
	s_waitcnt vmcnt(8)
	s_waitcnt lgkmcnt(0)
	s_barrier
	v_mfma_f32_16x16x32_bf16 v[114:117], v[142:145], v[204:207], v[114:117]
	v_mfma_f32_16x16x32_bf16 v[98:101], v[176:179], v[204:207], v[98:101]
	v_mfma_f32_16x16x32_bf16 v[82:85], v[142:145], v[212:215], v[82:85]
	v_mfma_f32_16x16x32_bf16 v[66:69], v[176:179], v[212:215], v[66:69]
	v_mfma_f32_16x16x32_bf16 v[50:53], v[142:145], v[220:223], v[50:53]
	v_mfma_f32_16x16x32_bf16 v[34:37], v[176:179], v[220:223], v[34:37]
	v_mfma_f32_16x16x32_bf16 v[18:21], v[142:145], v[228:231], v[18:21]
	v_mfma_f32_16x16x32_bf16 v[6:9], v[176:179], v[228:231], v[6:9]
	v_mfma_f32_16x16x32_bf16 v[106:109], v[184:187], v[204:207], v[106:109]
	v_mfma_f32_16x16x32_bf16 v[94:97], v[196:199], v[204:207], v[94:97]
	v_mfma_f32_16x16x32_bf16 v[78:81], v[184:187], v[212:215], v[78:81]
	v_mfma_f32_16x16x32_bf16 v[62:65], v[196:199], v[212:215], v[62:65]
	v_mfma_f32_16x16x32_bf16 v[46:49], v[184:187], v[220:223], v[46:49]
	v_mfma_f32_16x16x32_bf16 v[30:33], v[196:199], v[220:223], v[30:33]
	v_mfma_f32_16x16x32_bf16 v[14:17], v[184:187], v[228:231], v[14:17]
	v_mfma_f32_16x16x32_bf16 v[2:5], v[196:199], v[228:231], v[2:5]
	v_mfma_f32_16x16x32_bf16 v[114:117], v[172:175], v[208:211], v[114:117]
	v_mfma_f32_16x16x32_bf16 v[98:101], v[180:183], v[208:211], v[98:101]
	v_mfma_f32_16x16x32_bf16 v[82:85], v[172:175], v[216:219], v[82:85]
	v_mfma_f32_16x16x32_bf16 v[66:69], v[180:183], v[216:219], v[66:69]
	v_mfma_f32_16x16x32_bf16 v[50:53], v[172:175], v[224:227], v[50:53]
	v_mfma_f32_16x16x32_bf16 v[34:37], v[180:183], v[224:227], v[34:37]
	v_mfma_f32_16x16x32_bf16 v[18:21], v[172:175], v[232:235], v[18:21]
	v_mfma_f32_16x16x32_bf16 v[6:9], v[180:183], v[232:235], v[6:9]
	v_mfma_f32_16x16x32_bf16 v[106:109], v[188:191], v[208:211], v[106:109]
	v_mfma_f32_16x16x32_bf16 v[94:97], v[200:203], v[208:211], v[94:97]
	v_mfma_f32_16x16x32_bf16 v[78:81], v[188:191], v[216:219], v[78:81]
	v_mfma_f32_16x16x32_bf16 v[62:65], v[200:203], v[216:219], v[62:65]
	v_mfma_f32_16x16x32_bf16 v[46:49], v[188:191], v[224:227], v[46:49]
	v_mfma_f32_16x16x32_bf16 v[30:33], v[200:203], v[224:227], v[30:33]
	v_mfma_f32_16x16x32_bf16 v[14:17], v[188:191], v[232:235], v[14:17]
	v_mfma_f32_16x16x32_bf16 v[2:5], v[200:203], v[232:235], v[2:5]
	s_barrier
	v_add_u32_e32 v154, 0x18000, v141
	v_add_u32_e32 v141, 0x1c000, v141
	ds_read_b128 v[142:145], v154
	ds_read_b128 v[172:175], v154 offset:1024
	ds_read_b128 v[176:179], v154 offset:2048
	ds_read_b128 v[180:183], v154 offset:3072
	ds_read_b128 v[184:187], v141
	ds_read_b128 v[188:191], v141 offset:1024
	ds_read_b128 v[196:199], v141 offset:2048
	ds_read_b128 v[200:203], v141 offset:3072
	s_mov_b32 m0, s71
	ds_read_b128 v[204:207], v153 offset:32768
	ds_read_b128 v[208:211], v153 offset:33792
	ds_read_b128 v[212:215], v153 offset:34816
	ds_read_b128 v[216:219], v153 offset:35840
	ds_read_b128 v[220:223], v153 offset:36864
	ds_read_b128 v[224:227], v153 offset:37888
	ds_read_b128 v[228:231], v153 offset:38912
	ds_read_b128 v[232:235], v153 offset:39936
	buffer_load_dwordx4 v140, s[8:11], s45 offen lds
	s_mov_b32 m0, s72
	s_nop 0
	buffer_load_dwordx4 v139, s[8:11], s45 offen lds
	s_waitcnt vmcnt(8)
	s_waitcnt lgkmcnt(0)
	s_barrier
	v_mfma_f32_16x16x32_bf16 v[126:129], v[142:145], v[204:207], v[126:129]
	v_mfma_f32_16x16x32_bf16 v[122:125], v[176:179], v[204:207], v[122:125]
	v_mfma_f32_16x16x32_bf16 v[102:105], v[142:145], v[212:215], v[102:105]
	v_mfma_f32_16x16x32_bf16 v[90:93], v[176:179], v[212:215], v[90:93]
	v_mfma_f32_16x16x32_bf16 v[70:73], v[142:145], v[220:223], v[70:73]
	v_mfma_f32_16x16x32_bf16 v[58:61], v[176:179], v[220:223], v[58:61]
	v_mfma_f32_16x16x32_bf16 v[38:41], v[142:145], v[228:231], v[38:41]
	v_mfma_f32_16x16x32_bf16 v[26:29], v[176:179], v[228:231], v[26:29]
	v_mfma_f32_16x16x32_bf16 v[118:121], v[184:187], v[204:207], v[118:121]
	v_mfma_f32_16x16x32_bf16 v[110:113], v[196:199], v[204:207], v[110:113]
	v_mfma_f32_16x16x32_bf16 v[86:89], v[184:187], v[212:215], v[86:89]
	v_mfma_f32_16x16x32_bf16 v[74:77], v[196:199], v[212:215], v[74:77]
	v_mfma_f32_16x16x32_bf16 v[54:57], v[184:187], v[220:223], v[54:57]
	v_mfma_f32_16x16x32_bf16 v[42:45], v[196:199], v[220:223], v[42:45]
	v_mfma_f32_16x16x32_bf16 v[22:25], v[184:187], v[228:231], v[22:25]
	v_mfma_f32_16x16x32_bf16 v[10:13], v[196:199], v[228:231], v[10:13]
	v_mfma_f32_16x16x32_bf16 v[126:129], v[172:175], v[208:211], v[126:129]
	v_mfma_f32_16x16x32_bf16 v[122:125], v[180:183], v[208:211], v[122:125]
	v_mfma_f32_16x16x32_bf16 v[102:105], v[172:175], v[216:219], v[102:105]
	v_mfma_f32_16x16x32_bf16 v[90:93], v[180:183], v[216:219], v[90:93]
	v_mfma_f32_16x16x32_bf16 v[70:73], v[172:175], v[224:227], v[70:73]
	v_mfma_f32_16x16x32_bf16 v[58:61], v[180:183], v[224:227], v[58:61]
	v_mfma_f32_16x16x32_bf16 v[38:41], v[172:175], v[232:235], v[38:41]
	v_mfma_f32_16x16x32_bf16 v[26:29], v[180:183], v[232:235], v[26:29]
	v_mfma_f32_16x16x32_bf16 v[118:121], v[188:191], v[208:211], v[118:121]
	v_mfma_f32_16x16x32_bf16 v[110:113], v[200:203], v[208:211], v[110:113]
	v_mfma_f32_16x16x32_bf16 v[86:89], v[188:191], v[216:219], v[86:89]
	v_mfma_f32_16x16x32_bf16 v[74:77], v[200:203], v[216:219], v[74:77]
	v_mfma_f32_16x16x32_bf16 v[54:57], v[188:191], v[224:227], v[54:57]
	v_mfma_f32_16x16x32_bf16 v[42:45], v[200:203], v[224:227], v[42:45]
	v_mfma_f32_16x16x32_bf16 v[22:25], v[188:191], v[232:235], v[22:25]
	v_mfma_f32_16x16x32_bf16 v[10:13], v[200:203], v[232:235], v[10:13]
	s_barrier
	s_mov_b32 m0, s73
	s_add_i32 s15, s14, 0x80
	ds_read_b128 v[204:207], v153 offset:49152
	ds_read_b128 v[208:211], v153 offset:50176
	ds_read_b128 v[212:215], v153 offset:51200
	ds_read_b128 v[216:219], v153 offset:52224
	ds_read_b128 v[220:223], v153 offset:53248
	ds_read_b128 v[224:227], v153 offset:54272
	ds_read_b128 v[228:231], v153 offset:55296
	ds_read_b128 v[232:235], v153 offset:56320
	buffer_load_dwordx4 v151, s[16:19], s15 offen lds
	s_mov_b32 m0, s74
	s_add_i32 s14, s14, 0x80080
	buffer_load_dwordx4 v158, s[16:19], s15 offen lds
	s_mov_b32 m0, s77
	s_bitset1_b32 s45, 7
	buffer_load_dwordx4 v151, s[16:19], s14 offen lds
	s_mov_b32 m0, s78
	s_nop 0
	buffer_load_dwordx4 v158, s[16:19], s14 offen lds
	s_mov_b32 m0, s75
	s_nop 0
	buffer_load_dwordx4 v138, s[8:11], s45 offen lds
	s_mov_b32 m0, s76
	s_nop 0
	buffer_load_dwordx4 v137, s[8:11], s45 offen lds
	s_add_i32 s44, s44, 2
	s_cmp_gt_u32 s44, 29
	s_waitcnt vmcnt(8)
	s_waitcnt lgkmcnt(0)
	s_barrier
	v_mfma_f32_16x16x32_bf16 v[114:117], v[142:145], v[204:207], v[114:117]
	v_mfma_f32_16x16x32_bf16 v[98:101], v[176:179], v[204:207], v[98:101]
	v_mfma_f32_16x16x32_bf16 v[82:85], v[142:145], v[212:215], v[82:85]
	v_mfma_f32_16x16x32_bf16 v[66:69], v[176:179], v[212:215], v[66:69]
	v_mfma_f32_16x16x32_bf16 v[50:53], v[142:145], v[220:223], v[50:53]
	v_mfma_f32_16x16x32_bf16 v[34:37], v[176:179], v[220:223], v[34:37]
	v_mfma_f32_16x16x32_bf16 v[18:21], v[142:145], v[228:231], v[18:21]
	v_mfma_f32_16x16x32_bf16 v[6:9], v[176:179], v[228:231], v[6:9]
	v_mfma_f32_16x16x32_bf16 v[106:109], v[184:187], v[204:207], v[106:109]
	v_mfma_f32_16x16x32_bf16 v[94:97], v[196:199], v[204:207], v[94:97]
	v_mfma_f32_16x16x32_bf16 v[78:81], v[184:187], v[212:215], v[78:81]
	v_mfma_f32_16x16x32_bf16 v[62:65], v[196:199], v[212:215], v[62:65]
	v_mfma_f32_16x16x32_bf16 v[46:49], v[184:187], v[220:223], v[46:49]
	v_mfma_f32_16x16x32_bf16 v[30:33], v[196:199], v[220:223], v[30:33]
	v_mfma_f32_16x16x32_bf16 v[14:17], v[184:187], v[228:231], v[14:17]
	v_mfma_f32_16x16x32_bf16 v[2:5], v[196:199], v[228:231], v[2:5]
	v_mfma_f32_16x16x32_bf16 v[114:117], v[172:175], v[208:211], v[114:117]
	v_mfma_f32_16x16x32_bf16 v[98:101], v[180:183], v[208:211], v[98:101]
	v_mfma_f32_16x16x32_bf16 v[82:85], v[172:175], v[216:219], v[82:85]
	v_mfma_f32_16x16x32_bf16 v[66:69], v[180:183], v[216:219], v[66:69]
	v_mfma_f32_16x16x32_bf16 v[50:53], v[172:175], v[224:227], v[50:53]
	v_mfma_f32_16x16x32_bf16 v[34:37], v[180:183], v[224:227], v[34:37]
	v_mfma_f32_16x16x32_bf16 v[18:21], v[172:175], v[232:235], v[18:21]
	v_mfma_f32_16x16x32_bf16 v[6:9], v[180:183], v[232:235], v[6:9]
	v_mfma_f32_16x16x32_bf16 v[106:109], v[188:191], v[208:211], v[106:109]
	v_mfma_f32_16x16x32_bf16 v[94:97], v[200:203], v[208:211], v[94:97]
	v_mfma_f32_16x16x32_bf16 v[78:81], v[188:191], v[216:219], v[78:81]
	v_mfma_f32_16x16x32_bf16 v[62:65], v[200:203], v[216:219], v[62:65]
	v_mfma_f32_16x16x32_bf16 v[46:49], v[188:191], v[224:227], v[46:49]
	v_mfma_f32_16x16x32_bf16 v[30:33], v[200:203], v[224:227], v[30:33]
	v_mfma_f32_16x16x32_bf16 v[14:17], v[188:191], v[232:235], v[14:17]
	v_mfma_f32_16x16x32_bf16 v[2:5], v[200:203], v[232:235], v[2:5]
	s_barrier
	s_cbranch_scc1 .LBB0_1248
	s_mov_b64 s[18:19], s[38:39]
	s_branch .LBB0_1244

.LBB0_1456:
	ds_read_b128 v[66:69], v159
	ds_read_b128 v[70:73], v159 offset:1024
	ds_read_b128 v[74:77], v159 offset:2048
	ds_read_b128 v[78:81], v159 offset:3072
	ds_read_b128 v[82:85], v160
	ds_read_b128 v[86:89], v160 offset:1024
	ds_read_b128 v[90:93], v160 offset:2048
	ds_read_b128 v[94:97], v160 offset:3072
	s_add_i32 s10, s44, s48
	s_sub_i32 s10, s10, s4
	s_add_i32 s47, s46, s48
	s_add_i32 s10, s10, 0x7ff80
	s_cmp_eq_u32 s45, 28
	s_cselect_b32 s50, 0, s48
	s_mov_b32 m0, s67
	ds_read_b128 v[98:101], v161
	ds_read_b128 v[102:105], v161 offset:1024
	ds_read_b128 v[106:109], v161 offset:2048
	ds_read_b128 v[110:113], v161 offset:3072
	ds_read_b128 v[114:117], v161 offset:4096
	ds_read_b128 v[118:121], v161 offset:5120
	ds_read_b128 v[122:125], v161 offset:6144
	ds_read_b128 v[126:129], v161 offset:7168
	buffer_load_dwordx4 v1, s[4:7], s10 offen lds
	s_mov_b32 m0, s68
	s_nop 0
	buffer_load_dwordx4 v153, s[4:7], s10 offen lds
	s_waitcnt vmcnt(8)
	s_waitcnt lgkmcnt(0)
	s_barrier
	v_mfma_f32_16x16x32_bf16 v[62:65], v[66:69], v[98:101], v[62:65]
	v_mfma_f32_16x16x32_bf16 v[58:61], v[74:77], v[98:101], v[58:61]
	v_mfma_f32_16x16x32_bf16 v[54:57], v[66:69], v[106:109], v[54:57]
	v_mfma_f32_16x16x32_bf16 v[50:53], v[74:77], v[106:109], v[50:53]
	v_mfma_f32_16x16x32_bf16 v[38:41], v[66:69], v[114:117], v[38:41]
	v_mfma_f32_16x16x32_bf16 v[34:37], v[74:77], v[114:117], v[34:37]
	v_mfma_f32_16x16x32_bf16 v[22:25], v[66:69], v[122:125], v[22:25]
	v_mfma_f32_16x16x32_bf16 v[18:21], v[74:77], v[122:125], v[18:21]
	v_mfma_f32_16x16x32_bf16 v[46:49], v[82:85], v[98:101], v[46:49]
	v_mfma_f32_16x16x32_bf16 v[42:45], v[90:93], v[98:101], v[42:45]
	v_mfma_f32_16x16x32_bf16 v[30:33], v[82:85], v[106:109], v[30:33]
	v_mfma_f32_16x16x32_bf16 v[26:29], v[90:93], v[106:109], v[26:29]
	v_mfma_f32_16x16x32_bf16 v[14:17], v[82:85], v[114:117], v[14:17]
	v_mfma_f32_16x16x32_bf16 v[10:13], v[90:93], v[114:117], v[10:13]
	v_mfma_f32_16x16x32_bf16 v[6:9], v[82:85], v[122:125], v[6:9]
	v_mfma_f32_16x16x32_bf16 v[2:5], v[90:93], v[122:125], v[2:5]
	v_mfma_f32_16x16x32_bf16 v[62:65], v[70:73], v[102:105], v[62:65]
	v_mfma_f32_16x16x32_bf16 v[58:61], v[78:81], v[102:105], v[58:61]
	v_mfma_f32_16x16x32_bf16 v[54:57], v[70:73], v[110:113], v[54:57]
	v_mfma_f32_16x16x32_bf16 v[50:53], v[78:81], v[110:113], v[50:53]
	v_mfma_f32_16x16x32_bf16 v[38:41], v[70:73], v[118:121], v[38:41]
	v_mfma_f32_16x16x32_bf16 v[34:37], v[78:81], v[118:121], v[34:37]
	v_mfma_f32_16x16x32_bf16 v[22:25], v[70:73], v[126:129], v[22:25]
	v_mfma_f32_16x16x32_bf16 v[18:21], v[78:81], v[126:129], v[18:21]
	v_mfma_f32_16x16x32_bf16 v[46:49], v[86:89], v[102:105], v[46:49]
	v_mfma_f32_16x16x32_bf16 v[42:45], v[94:97], v[102:105], v[42:45]
	v_mfma_f32_16x16x32_bf16 v[30:33], v[86:89], v[110:113], v[30:33]
	v_mfma_f32_16x16x32_bf16 v[26:29], v[94:97], v[110:113], v[26:29]
	v_mfma_f32_16x16x32_bf16 v[14:17], v[86:89], v[118:121], v[14:17]
	v_mfma_f32_16x16x32_bf16 v[10:13], v[94:97], v[118:121], v[10:13]
	v_mfma_f32_16x16x32_bf16 v[6:9], v[86:89], v[126:129], v[6:9]
	v_mfma_f32_16x16x32_bf16 v[2:5], v[94:97], v[126:129], v[2:5]
	s_barrier
	s_cselect_b32 s47, s31, s47
	s_mov_b32 m0, s53
	s_mov_b32 s10, s6
	s_mov_b32 s11, s7
	s_cselect_b32 s51, s27, s44
	s_sub_i32 s47, s47, s8
	buffer_load_dwordx4 v152, s[8:11], s47 offen lds
	s_mov_b32 m0, s54
	s_add_i32 s73, s47, 0x80000
	buffer_load_dwordx4 v154, s[8:11], s47 offen lds
	s_mov_b32 m0, s55
	s_add_i32 s51, s51, s50
	buffer_load_dwordx4 v152, s[8:11], s73 offen lds
	s_mov_b32 m0, s56
	s_sub_i32 s50, s51, s4
	buffer_load_dwordx4 v154, s[8:11], s73 offen lds
	s_mov_b32 m0, s43
	s_nop 0
	buffer_load_dwordx4 v1, s[4:7], s50 offen lds
	s_mov_b32 m0, s57
	s_nop 0
	buffer_load_dwordx4 v153, s[4:7], s50 offen lds
	s_waitcnt vmcnt(8)
	s_waitcnt lgkmcnt(0)
	s_barrier
	s_barrier
	ds_read_b128 v[66:69], v162
	ds_read_b128 v[70:73], v162 offset:1024
	ds_read_b128 v[74:77], v162 offset:2048
	ds_read_b128 v[78:81], v162 offset:3072
	ds_read_b128 v[82:85], v163
	ds_read_b128 v[86:89], v163 offset:1024
	ds_read_b128 v[90:93], v163 offset:2048
	ds_read_b128 v[94:97], v163 offset:3072
	s_add_i32 s51, s50, 0x80000
	s_mov_b32 m0, s58
	ds_read_b128 v[98:101], v161 offset:32768
	ds_read_b128 v[102:105], v161 offset:33792
	ds_read_b128 v[106:109], v161 offset:34816
	ds_read_b128 v[110:113], v161 offset:35840
	ds_read_b128 v[114:117], v161 offset:36864
	ds_read_b128 v[118:121], v161 offset:37888
	ds_read_b128 v[122:125], v161 offset:38912
	ds_read_b128 v[126:129], v161 offset:39936
	buffer_load_dwordx4 v1, s[4:7], s51 offen lds
	s_mov_b32 m0, s59
	s_nop 0
	buffer_load_dwordx4 v153, s[4:7], s51 offen lds
	s_waitcnt vmcnt(8)
	s_waitcnt lgkmcnt(0)
	s_barrier
	v_mfma_f32_16x16x32_bf16 v[62:65], v[66:69], v[98:101], v[62:65]
	v_mfma_f32_16x16x32_bf16 v[58:61], v[74:77], v[98:101], v[58:61]
	v_mfma_f32_16x16x32_bf16 v[54:57], v[66:69], v[106:109], v[54:57]
	v_mfma_f32_16x16x32_bf16 v[50:53], v[74:77], v[106:109], v[50:53]
	v_mfma_f32_16x16x32_bf16 v[38:41], v[66:69], v[114:117], v[38:41]
	v_mfma_f32_16x16x32_bf16 v[34:37], v[74:77], v[114:117], v[34:37]
	v_mfma_f32_16x16x32_bf16 v[22:25], v[66:69], v[122:125], v[22:25]
	v_mfma_f32_16x16x32_bf16 v[18:21], v[74:77], v[122:125], v[18:21]
	v_mfma_f32_16x16x32_bf16 v[46:49], v[82:85], v[98:101], v[46:49]
	v_mfma_f32_16x16x32_bf16 v[42:45], v[90:93], v[98:101], v[42:45]
	v_mfma_f32_16x16x32_bf16 v[30:33], v[82:85], v[106:109], v[30:33]
	v_mfma_f32_16x16x32_bf16 v[26:29], v[90:93], v[106:109], v[26:29]
	v_mfma_f32_16x16x32_bf16 v[14:17], v[82:85], v[114:117], v[14:17]
	v_mfma_f32_16x16x32_bf16 v[10:13], v[90:93], v[114:117], v[10:13]
	v_mfma_f32_16x16x32_bf16 v[6:9], v[82:85], v[122:125], v[6:9]
	v_mfma_f32_16x16x32_bf16 v[2:5], v[90:93], v[122:125], v[2:5]
	v_mfma_f32_16x16x32_bf16 v[62:65], v[70:73], v[102:105], v[62:65]
	v_mfma_f32_16x16x32_bf16 v[58:61], v[78:81], v[102:105], v[58:61]
	v_mfma_f32_16x16x32_bf16 v[54:57], v[70:73], v[110:113], v[54:57]
	v_mfma_f32_16x16x32_bf16 v[50:53], v[78:81], v[110:113], v[50:53]
	v_mfma_f32_16x16x32_bf16 v[38:41], v[70:73], v[118:121], v[38:41]
	v_mfma_f32_16x16x32_bf16 v[34:37], v[78:81], v[118:121], v[34:37]
	v_mfma_f32_16x16x32_bf16 v[22:25], v[70:73], v[126:129], v[22:25]
	v_mfma_f32_16x16x32_bf16 v[18:21], v[78:81], v[126:129], v[18:21]
	v_mfma_f32_16x16x32_bf16 v[46:49], v[86:89], v[102:105], v[46:49]
	v_mfma_f32_16x16x32_bf16 v[42:45], v[94:97], v[102:105], v[42:45]
	v_mfma_f32_16x16x32_bf16 v[30:33], v[86:89], v[110:113], v[30:33]
	v_mfma_f32_16x16x32_bf16 v[26:29], v[94:97], v[110:113], v[26:29]
	v_mfma_f32_16x16x32_bf16 v[14:17], v[86:89], v[118:121], v[14:17]
	v_mfma_f32_16x16x32_bf16 v[10:13], v[94:97], v[118:121], v[10:13]
	v_mfma_f32_16x16x32_bf16 v[6:9], v[86:89], v[126:129], v[6:9]
	v_mfma_f32_16x16x32_bf16 v[2:5], v[94:97], v[126:129], v[2:5]
	s_barrier
	s_mov_b32 m0, s61
	s_add_i32 s51, s47, 0x80
	buffer_load_dwordx4 v152, s[8:11], s51 offen lds
	s_mov_b32 m0, s62
	s_add_i32 s47, s47, 0x80080
	buffer_load_dwordx4 v154, s[8:11], s51 offen lds
	s_mov_b32 m0, s65
	s_addk_i32 s50, 0x80
	buffer_load_dwordx4 v152, s[8:11], s47 offen lds
	s_mov_b32 m0, s66
	s_nop 0
	buffer_load_dwordx4 v154, s[8:11], s47 offen lds
	s_mov_b32 m0, s63
	s_nop 0
	buffer_load_dwordx4 v1, s[4:7], s50 offen lds
	s_mov_b32 m0, s64
	s_nop 0
	buffer_load_dwordx4 v153, s[4:7], s50 offen lds
	s_add_i32 s45, s45, 2
	s_add_u32 s48, s48, 0x100
	s_addc_u32 s49, s49, 0
	s_cmp_lt_u32 s45, 30
	s_waitcnt vmcnt(8)
	s_waitcnt lgkmcnt(0)
	s_barrier
	s_barrier
	s_cbranch_scc1 .LBB0_1456
	s_mov_b64 s[10:11], 0

.LBB0_1460:
	ds_read_b128 v[132:135], v159
	ds_read_b128 v[136:139], v159 offset:1024
	ds_read_b128 v[140:143], v159 offset:2048
	ds_read_b128 v[164:167], v159 offset:3072
	ds_read_b128 v[168:171], v160
	ds_read_b128 v[172:175], v160 offset:1024
	ds_read_b128 v[176:179], v160 offset:2048
	ds_read_b128 v[180:183], v160 offset:3072
	s_add_i32 s10, s44, s48
	s_sub_i32 s10, s10, s4
	s_add_i32 s47, s46, s48
	s_add_i32 s10, s10, 0x7ff80
	s_cmp_eq_u32 s45, 28
	s_cselect_b32 s50, 0, s48
	s_mov_b32 m0, s67
	ds_read_b128 v[184:187], v161
	ds_read_b128 v[188:191], v161 offset:1024
	ds_read_b128 v[196:199], v161 offset:2048
	ds_read_b128 v[200:203], v161 offset:3072
	ds_read_b128 v[204:207], v161 offset:4096
	ds_read_b128 v[208:211], v161 offset:5120
	ds_read_b128 v[212:215], v161 offset:6144
	ds_read_b128 v[216:219], v161 offset:7168
	buffer_load_dwordx4 v1, s[4:7], s10 offen lds
	s_mov_b32 m0, s68
	s_nop 0
	buffer_load_dwordx4 v153, s[4:7], s10 offen lds
	s_waitcnt vmcnt(8)
	s_waitcnt lgkmcnt(0)
	s_barrier
	v_mfma_f32_16x16x32_bf16 v[62:65], v[132:135], v[184:187], v[62:65]
	v_mfma_f32_16x16x32_bf16 v[58:61], v[140:143], v[184:187], v[58:61]
	v_mfma_f32_16x16x32_bf16 v[54:57], v[132:135], v[196:199], v[54:57]
	v_mfma_f32_16x16x32_bf16 v[50:53], v[140:143], v[196:199], v[50:53]
	v_mfma_f32_16x16x32_bf16 v[38:41], v[132:135], v[204:207], v[38:41]
	v_mfma_f32_16x16x32_bf16 v[34:37], v[140:143], v[204:207], v[34:37]
	v_mfma_f32_16x16x32_bf16 v[22:25], v[132:135], v[212:215], v[22:25]
	v_mfma_f32_16x16x32_bf16 v[18:21], v[140:143], v[212:215], v[18:21]
	v_mfma_f32_16x16x32_bf16 v[46:49], v[168:171], v[184:187], v[46:49]
	v_mfma_f32_16x16x32_bf16 v[42:45], v[176:179], v[184:187], v[42:45]
	v_mfma_f32_16x16x32_bf16 v[30:33], v[168:171], v[196:199], v[30:33]
	v_mfma_f32_16x16x32_bf16 v[26:29], v[176:179], v[196:199], v[26:29]
	v_mfma_f32_16x16x32_bf16 v[14:17], v[168:171], v[204:207], v[14:17]
	v_mfma_f32_16x16x32_bf16 v[10:13], v[176:179], v[204:207], v[10:13]
	v_mfma_f32_16x16x32_bf16 v[6:9], v[168:171], v[212:215], v[6:9]
	v_mfma_f32_16x16x32_bf16 v[2:5], v[176:179], v[212:215], v[2:5]
	v_mfma_f32_16x16x32_bf16 v[62:65], v[136:139], v[188:191], v[62:65]
	v_mfma_f32_16x16x32_bf16 v[58:61], v[164:167], v[188:191], v[58:61]
	v_mfma_f32_16x16x32_bf16 v[54:57], v[136:139], v[200:203], v[54:57]
	v_mfma_f32_16x16x32_bf16 v[50:53], v[164:167], v[200:203], v[50:53]
	v_mfma_f32_16x16x32_bf16 v[38:41], v[136:139], v[208:211], v[38:41]
	v_mfma_f32_16x16x32_bf16 v[34:37], v[164:167], v[208:211], v[34:37]
	v_mfma_f32_16x16x32_bf16 v[22:25], v[136:139], v[216:219], v[22:25]
	v_mfma_f32_16x16x32_bf16 v[18:21], v[164:167], v[216:219], v[18:21]
	v_mfma_f32_16x16x32_bf16 v[46:49], v[172:175], v[188:191], v[46:49]
	v_mfma_f32_16x16x32_bf16 v[42:45], v[180:183], v[188:191], v[42:45]
	v_mfma_f32_16x16x32_bf16 v[30:33], v[172:175], v[200:203], v[30:33]
	v_mfma_f32_16x16x32_bf16 v[26:29], v[180:183], v[200:203], v[26:29]
	v_mfma_f32_16x16x32_bf16 v[14:17], v[172:175], v[208:211], v[14:17]
	v_mfma_f32_16x16x32_bf16 v[10:13], v[180:183], v[208:211], v[10:13]
	v_mfma_f32_16x16x32_bf16 v[6:9], v[172:175], v[216:219], v[6:9]
	v_mfma_f32_16x16x32_bf16 v[2:5], v[180:183], v[216:219], v[2:5]
	s_barrier
	s_cselect_b32 s47, s31, s47
	s_mov_b32 m0, s53
	s_mov_b32 s10, s6
	s_mov_b32 s11, s7
	s_cselect_b32 s51, s27, s44
	s_sub_i32 s47, s47, s8
	ds_read_b128 v[184:187], v161 offset:16384
	ds_read_b128 v[188:191], v161 offset:17408
	ds_read_b128 v[196:199], v161 offset:18432
	ds_read_b128 v[200:203], v161 offset:19456
	ds_read_b128 v[204:207], v161 offset:20480
	ds_read_b128 v[208:211], v161 offset:21504
	ds_read_b128 v[212:215], v161 offset:22528
	ds_read_b128 v[216:219], v161 offset:23552
	buffer_load_dwordx4 v152, s[8:11], s47 offen lds
	s_mov_b32 m0, s54
	s_add_i32 s73, s47, 0x80000
	buffer_load_dwordx4 v154, s[8:11], s47 offen lds
	s_mov_b32 m0, s55
	s_add_i32 s51, s51, s50
	buffer_load_dwordx4 v152, s[8:11], s73 offen lds
	s_mov_b32 m0, s56
	s_sub_i32 s50, s51, s4
	buffer_load_dwordx4 v154, s[8:11], s73 offen lds
	s_mov_b32 m0, s43
	s_nop 0
	buffer_load_dwordx4 v1, s[4:7], s50 offen lds
	s_mov_b32 m0, s57
	s_nop 0
	buffer_load_dwordx4 v153, s[4:7], s50 offen lds
	s_waitcnt vmcnt(8)
	s_waitcnt lgkmcnt(0)
	s_barrier
	v_mfma_f32_16x16x32_bf16 v[126:129], v[132:135], v[184:187], v[126:129]
	v_mfma_f32_16x16x32_bf16 v[122:125], v[140:143], v[184:187], v[122:125]
	v_mfma_f32_16x16x32_bf16 v[110:113], v[132:135], v[196:199], v[110:113]
	v_mfma_f32_16x16x32_bf16 v[106:109], v[140:143], v[196:199], v[106:109]
	v_mfma_f32_16x16x32_bf16 v[94:97], v[132:135], v[204:207], v[94:97]
	v_mfma_f32_16x16x32_bf16 v[90:93], v[140:143], v[204:207], v[90:93]
	v_mfma_f32_16x16x32_bf16 v[78:81], v[132:135], v[212:215], v[78:81]
	v_mfma_f32_16x16x32_bf16 v[74:77], v[140:143], v[212:215], v[74:77]
	v_mfma_f32_16x16x32_bf16 v[118:121], v[168:171], v[184:187], v[118:121]
	v_mfma_f32_16x16x32_bf16 v[114:117], v[176:179], v[184:187], v[114:117]
	v_mfma_f32_16x16x32_bf16 v[102:105], v[168:171], v[196:199], v[102:105]
	v_mfma_f32_16x16x32_bf16 v[98:101], v[176:179], v[196:199], v[98:101]
	v_mfma_f32_16x16x32_bf16 v[86:89], v[168:171], v[204:207], v[86:89]
	v_mfma_f32_16x16x32_bf16 v[82:85], v[176:179], v[204:207], v[82:85]
	v_mfma_f32_16x16x32_bf16 v[70:73], v[168:171], v[212:215], v[70:73]
	v_mfma_f32_16x16x32_bf16 v[66:69], v[176:179], v[212:215], v[66:69]
	v_mfma_f32_16x16x32_bf16 v[126:129], v[136:139], v[188:191], v[126:129]
	v_mfma_f32_16x16x32_bf16 v[122:125], v[164:167], v[188:191], v[122:125]
	v_mfma_f32_16x16x32_bf16 v[110:113], v[136:139], v[200:203], v[110:113]
	v_mfma_f32_16x16x32_bf16 v[106:109], v[164:167], v[200:203], v[106:109]
	v_mfma_f32_16x16x32_bf16 v[94:97], v[136:139], v[208:211], v[94:97]
	v_mfma_f32_16x16x32_bf16 v[90:93], v[164:167], v[208:211], v[90:93]
	v_mfma_f32_16x16x32_bf16 v[78:81], v[136:139], v[216:219], v[78:81]
	v_mfma_f32_16x16x32_bf16 v[74:77], v[164:167], v[216:219], v[74:77]
	v_mfma_f32_16x16x32_bf16 v[118:121], v[172:175], v[188:191], v[118:121]
	v_mfma_f32_16x16x32_bf16 v[114:117], v[180:183], v[188:191], v[114:117]
	v_mfma_f32_16x16x32_bf16 v[102:105], v[172:175], v[200:203], v[102:105]
	v_mfma_f32_16x16x32_bf16 v[98:101], v[180:183], v[200:203], v[98:101]
	v_mfma_f32_16x16x32_bf16 v[86:89], v[172:175], v[208:211], v[86:89]
	v_mfma_f32_16x16x32_bf16 v[82:85], v[180:183], v[208:211], v[82:85]
	v_mfma_f32_16x16x32_bf16 v[70:73], v[172:175], v[216:219], v[70:73]
	v_mfma_f32_16x16x32_bf16 v[66:69], v[180:183], v[216:219], v[66:69]
	s_barrier
	ds_read_b128 v[132:135], v162
	ds_read_b128 v[136:139], v162 offset:1024
	ds_read_b128 v[140:143], v162 offset:2048
	ds_read_b128 v[164:167], v162 offset:3072
	ds_read_b128 v[168:171], v163
	ds_read_b128 v[172:175], v163 offset:1024
	ds_read_b128 v[176:179], v163 offset:2048
	ds_read_b128 v[180:183], v163 offset:3072
	s_add_i32 s51, s50, 0x80000
	s_mov_b32 m0, s58
	ds_read_b128 v[184:187], v161 offset:32768
	ds_read_b128 v[188:191], v161 offset:33792
	ds_read_b128 v[196:199], v161 offset:34816
	ds_read_b128 v[200:203], v161 offset:35840
	ds_read_b128 v[204:207], v161 offset:36864
	ds_read_b128 v[208:211], v161 offset:37888
	ds_read_b128 v[212:215], v161 offset:38912
	ds_read_b128 v[216:219], v161 offset:39936
	buffer_load_dwordx4 v1, s[4:7], s51 offen lds
	s_mov_b32 m0, s59
	s_nop 0
	buffer_load_dwordx4 v153, s[4:7], s51 offen lds
	s_waitcnt vmcnt(8)
	s_waitcnt lgkmcnt(0)
	s_barrier
	v_mfma_f32_16x16x32_bf16 v[62:65], v[132:135], v[184:187], v[62:65]
	v_mfma_f32_16x16x32_bf16 v[58:61], v[140:143], v[184:187], v[58:61]
	v_mfma_f32_16x16x32_bf16 v[54:57], v[132:135], v[196:199], v[54:57]
	v_mfma_f32_16x16x32_bf16 v[50:53], v[140:143], v[196:199], v[50:53]
	v_mfma_f32_16x16x32_bf16 v[38:41], v[132:135], v[204:207], v[38:41]
	v_mfma_f32_16x16x32_bf16 v[34:37], v[140:143], v[204:207], v[34:37]
	v_mfma_f32_16x16x32_bf16 v[22:25], v[132:135], v[212:215], v[22:25]
	v_mfma_f32_16x16x32_bf16 v[18:21], v[140:143], v[212:215], v[18:21]
	v_mfma_f32_16x16x32_bf16 v[46:49], v[168:171], v[184:187], v[46:49]
	v_mfma_f32_16x16x32_bf16 v[42:45], v[176:179], v[184:187], v[42:45]
	v_mfma_f32_16x16x32_bf16 v[30:33], v[168:171], v[196:199], v[30:33]
	v_mfma_f32_16x16x32_bf16 v[26:29], v[176:179], v[196:199], v[26:29]
	v_mfma_f32_16x16x32_bf16 v[14:17], v[168:171], v[204:207], v[14:17]
	v_mfma_f32_16x16x32_bf16 v[10:13], v[176:179], v[204:207], v[10:13]
	v_mfma_f32_16x16x32_bf16 v[6:9], v[168:171], v[212:215], v[6:9]
	v_mfma_f32_16x16x32_bf16 v[2:5], v[176:179], v[212:215], v[2:5]
	v_mfma_f32_16x16x32_bf16 v[62:65], v[136:139], v[188:191], v[62:65]
	v_mfma_f32_16x16x32_bf16 v[58:61], v[164:167], v[188:191], v[58:61]
	v_mfma_f32_16x16x32_bf16 v[54:57], v[136:139], v[200:203], v[54:57]
	v_mfma_f32_16x16x32_bf16 v[50:53], v[164:167], v[200:203], v[50:53]
	v_mfma_f32_16x16x32_bf16 v[38:41], v[136:139], v[208:211], v[38:41]
	v_mfma_f32_16x16x32_bf16 v[34:37], v[164:167], v[208:211], v[34:37]
	v_mfma_f32_16x16x32_bf16 v[22:25], v[136:139], v[216:219], v[22:25]
	v_mfma_f32_16x16x32_bf16 v[18:21], v[164:167], v[216:219], v[18:21]
	v_mfma_f32_16x16x32_bf16 v[46:49], v[172:175], v[188:191], v[46:49]
	v_mfma_f32_16x16x32_bf16 v[42:45], v[180:183], v[188:191], v[42:45]
	v_mfma_f32_16x16x32_bf16 v[30:33], v[172:175], v[200:203], v[30:33]
	v_mfma_f32_16x16x32_bf16 v[26:29], v[180:183], v[200:203], v[26:29]
	v_mfma_f32_16x16x32_bf16 v[14:17], v[172:175], v[208:211], v[14:17]
	v_mfma_f32_16x16x32_bf16 v[10:13], v[180:183], v[208:211], v[10:13]
	v_mfma_f32_16x16x32_bf16 v[6:9], v[172:175], v[216:219], v[6:9]
	v_mfma_f32_16x16x32_bf16 v[2:5], v[180:183], v[216:219], v[2:5]
	s_barrier
	s_mov_b32 m0, s61
	s_add_i32 s51, s47, 0x80
	ds_read_b128 v[184:187], v161 offset:49152
	ds_read_b128 v[188:191], v161 offset:50176
	ds_read_b128 v[196:199], v161 offset:51200
	ds_read_b128 v[200:203], v161 offset:52224
	ds_read_b128 v[204:207], v161 offset:53248
	ds_read_b128 v[208:211], v161 offset:54272
	ds_read_b128 v[212:215], v161 offset:55296
	ds_read_b128 v[216:219], v161 offset:56320
	buffer_load_dwordx4 v152, s[8:11], s51 offen lds
	s_mov_b32 m0, s62
	s_add_i32 s47, s47, 0x80080
	buffer_load_dwordx4 v154, s[8:11], s51 offen lds
	s_mov_b32 m0, s65
	s_addk_i32 s50, 0x80
	buffer_load_dwordx4 v152, s[8:11], s47 offen lds
	s_mov_b32 m0, s66
	s_nop 0
	buffer_load_dwordx4 v154, s[8:11], s47 offen lds
	s_mov_b32 m0, s63
	s_nop 0
	buffer_load_dwordx4 v1, s[4:7], s50 offen lds
	s_mov_b32 m0, s64
	s_nop 0
	buffer_load_dwordx4 v153, s[4:7], s50 offen lds
	s_add_i32 s45, s45, 2
	s_add_u32 s48, s48, 0x100
	s_addc_u32 s49, s49, 0
	s_cmp_gt_u32 s45, 29
	s_waitcnt vmcnt(8)
	s_waitcnt lgkmcnt(0)
	s_barrier
	v_mfma_f32_16x16x32_bf16 v[126:129], v[132:135], v[184:187], v[126:129]
	v_mfma_f32_16x16x32_bf16 v[122:125], v[140:143], v[184:187], v[122:125]
	v_mfma_f32_16x16x32_bf16 v[110:113], v[132:135], v[196:199], v[110:113]
	v_mfma_f32_16x16x32_bf16 v[106:109], v[140:143], v[196:199], v[106:109]
	v_mfma_f32_16x16x32_bf16 v[94:97], v[132:135], v[204:207], v[94:97]
	v_mfma_f32_16x16x32_bf16 v[90:93], v[140:143], v[204:207], v[90:93]
	v_mfma_f32_16x16x32_bf16 v[78:81], v[132:135], v[212:215], v[78:81]
	v_mfma_f32_16x16x32_bf16 v[74:77], v[140:143], v[212:215], v[74:77]
	v_mfma_f32_16x16x32_bf16 v[118:121], v[168:171], v[184:187], v[118:121]
	v_mfma_f32_16x16x32_bf16 v[114:117], v[176:179], v[184:187], v[114:117]
	v_mfma_f32_16x16x32_bf16 v[102:105], v[168:171], v[196:199], v[102:105]
	v_mfma_f32_16x16x32_bf16 v[98:101], v[176:179], v[196:199], v[98:101]
	v_mfma_f32_16x16x32_bf16 v[86:89], v[168:171], v[204:207], v[86:89]
	v_mfma_f32_16x16x32_bf16 v[82:85], v[176:179], v[204:207], v[82:85]
	v_mfma_f32_16x16x32_bf16 v[70:73], v[168:171], v[212:215], v[70:73]
	v_mfma_f32_16x16x32_bf16 v[66:69], v[176:179], v[212:215], v[66:69]
	v_mfma_f32_16x16x32_bf16 v[126:129], v[136:139], v[188:191], v[126:129]
	v_mfma_f32_16x16x32_bf16 v[122:125], v[164:167], v[188:191], v[122:125]
	v_mfma_f32_16x16x32_bf16 v[110:113], v[136:139], v[200:203], v[110:113]
	v_mfma_f32_16x16x32_bf16 v[106:109], v[164:167], v[200:203], v[106:109]
	v_mfma_f32_16x16x32_bf16 v[94:97], v[136:139], v[208:211], v[94:97]
	v_mfma_f32_16x16x32_bf16 v[90:93], v[164:167], v[208:211], v[90:93]
	v_mfma_f32_16x16x32_bf16 v[78:81], v[136:139], v[216:219], v[78:81]
	v_mfma_f32_16x16x32_bf16 v[74:77], v[164:167], v[216:219], v[74:77]
	v_mfma_f32_16x16x32_bf16 v[118:121], v[172:175], v[188:191], v[118:121]
	v_mfma_f32_16x16x32_bf16 v[114:117], v[180:183], v[188:191], v[114:117]
	v_mfma_f32_16x16x32_bf16 v[102:105], v[172:175], v[200:203], v[102:105]
	v_mfma_f32_16x16x32_bf16 v[98:101], v[180:183], v[200:203], v[98:101]
	v_mfma_f32_16x16x32_bf16 v[86:89], v[172:175], v[208:211], v[86:89]
	v_mfma_f32_16x16x32_bf16 v[82:85], v[180:183], v[208:211], v[82:85]
	v_mfma_f32_16x16x32_bf16 v[70:73], v[172:175], v[216:219], v[70:73]
	v_mfma_f32_16x16x32_bf16 v[66:69], v[180:183], v[216:219], v[66:69]
	s_barrier
	s_cbranch_scc0 .LBB0_1460
